# P9 rope epilogue: all 16 cos/sin row vectors loaded at the first row group (rot waves) into idle VGPRs, later load blocks become register copies, per-group vmcnt waits (which waited on the previous gr
# speedup vs baseline: 1.0314x; 1.0039x over previous
;     __device__ __forceinline__ void operator()(const f32x4 (&acc)[2][2][4][2], const Unit& u, int wr, int wc, int fr, int fq) const {
;         const int row0 = u.pm * BM + wr * 64 + fr, col0 = u.pn * BM + wc * 32 + 8 * fq; const bool rot = (u.pn < 16) && (wc == 0);
; #pragma unroll
;         for (int ai = 0; ai < 2; ++ai)
; #pragma unroll
;             for (int m = 0; m < 4; ++m) { const int row = row0 + ai * HALF + m * 16; bf16_t* rowp = O + (size_t)row * ldc + col0;
;                 f32x4 cv = {1.f, 1.f, 1.f, 1.f}, sv = {0.f, 0.f, 0.f, 0.f};
;                 if (rot) { const int pos = row & (T - 1); cv = *(const f32x4*)(rc + pos * 16 + 4 * fq); sv = *(const f32x4*)(rs + pos * 16 + 4 * fq); }
.LBB0_797:
	v_mov_b32_e32 v0, v241
	s_nop 15
	s_nop 7
	s_lshl_b32 s8, s8, 8
	v_readfirstlane_b32 s9, v0
	s_bfe_u32 s39, s9, 0x20006
	s_ashr_i32 s9, s9, 2
	s_andn2_b32 s9, s9, 63
	s_add_i32 s9, s9, s8
	s_cmp_lt_i32 s46, 16
	v_and_or_b32 v24, v0, 15, s9
	s_cselect_b64 s[8:9], -1, 0
	s_cmp_eq_u32 s39, 0
	s_cselect_b64 s[48:49], -1, 0
	v_bfe_u32 v12, v0, 4, 2
	s_and_b64 s[48:49], s[8:9], s[48:49]
	v_lshlrev_b32_e32 v0, 2, v12
	v_cndmask_b32_e64 v2, 0, 1, s[48:49]
	v_cmp_ne_u32_e64 s[8:9], 1, v2
	s_andn2_b64 vcc, exec, s[48:49]
	v_lshlrev_b32_e32 v10, 2, v0
	s_cbranch_vccnz .LBB0_799
	v_lshlrev_b32_e32 v0, 6, v24
	v_and_b32_e32 v162, 0x1f3c0, v0
	v_lshl_add_u64 v[2:3], s[16:17], 0, v[162:163]
	v_mov_b32_e32 v11, v163
	v_lshl_add_u64 v[6:7], v[2:3], 0, v[10:11]
	v_lshl_add_u64 v[2:3], s[10:11], 0, v[162:163]
	v_lshl_add_u64 v[2:3], v[2:3], 0, v[10:11]
	global_load_dwordx4 v[2:5], v[2:3], off
	s_nop 0
	global_load_dwordx4 v[6:9], v[6:7], off
	v_add_u32_e32 v176, 16, v24
	v_lshlrev_b32_e32 v176, 6, v176
	v_and_b32_e32 v176, 0x1ffc0, v176
	v_mov_b32_e32 v177, 0
	v_lshl_add_u64 v[180:181], s[16:17], 0, v[176:177]
	v_lshl_add_u64 v[180:181], v[180:181], 0, v[10:11]
	v_lshl_add_u64 v[176:177], s[10:11], 0, v[176:177]
	v_lshl_add_u64 v[176:177], v[176:177], 0, v[10:11]
	global_load_dwordx4 v[176:179], v[176:177], off
	global_load_dwordx4 v[180:183], v[180:181], off
	v_add_u32_e32 v184, 32, v24
	v_lshlrev_b32_e32 v184, 6, v184
	v_and_b32_e32 v184, 0x1ffc0, v184
	v_mov_b32_e32 v185, 0
	v_lshl_add_u64 v[188:189], s[16:17], 0, v[184:185]
	v_lshl_add_u64 v[188:189], v[188:189], 0, v[10:11]
	v_lshl_add_u64 v[184:185], s[10:11], 0, v[184:185]
	v_lshl_add_u64 v[184:185], v[184:185], 0, v[10:11]
	global_load_dwordx4 v[184:187], v[184:185], off
	global_load_dwordx4 v[188:191], v[188:189], off
	v_add_u32_e32 v192, 48, v24
	v_lshlrev_b32_e32 v192, 6, v192
	v_and_b32_e32 v192, 0x1ffc0, v192
	v_mov_b32_e32 v193, 0
	v_lshl_add_u64 v[196:197], s[16:17], 0, v[192:193]
	v_lshl_add_u64 v[196:197], v[196:197], 0, v[10:11]
	v_lshl_add_u64 v[192:193], s[10:11], 0, v[192:193]
	v_lshl_add_u64 v[192:193], v[192:193], 0, v[10:11]
	global_load_dwordx4 v[192:195], v[192:193], off
	global_load_dwordx4 v[196:199], v[196:197], off
	v_add_u32_e32 v200, 128, v24
	v_lshlrev_b32_e32 v200, 6, v200
	v_and_b32_e32 v200, 0x1ffc0, v200
	v_mov_b32_e32 v201, 0
	v_lshl_add_u64 v[204:205], s[16:17], 0, v[200:201]
	v_lshl_add_u64 v[204:205], v[204:205], 0, v[10:11]
	v_lshl_add_u64 v[200:201], s[10:11], 0, v[200:201]
	v_lshl_add_u64 v[200:201], v[200:201], 0, v[10:11]
	global_load_dwordx4 v[200:203], v[200:201], off
	global_load_dwordx4 v[204:207], v[204:205], off
	v_add_u32_e32 v208, 144, v24
	v_lshlrev_b32_e32 v208, 6, v208
	v_and_b32_e32 v208, 0x1ffc0, v208
	v_mov_b32_e32 v209, 0
	v_lshl_add_u64 v[212:213], s[16:17], 0, v[208:209]
	v_lshl_add_u64 v[212:213], v[212:213], 0, v[10:11]
	v_lshl_add_u64 v[208:209], s[10:11], 0, v[208:209]
	v_lshl_add_u64 v[208:209], v[208:209], 0, v[10:11]
	global_load_dwordx4 v[208:211], v[208:209], off
	global_load_dwordx4 v[212:215], v[212:213], off
	v_add_u32_e32 v216, 160, v24
	v_lshlrev_b32_e32 v216, 6, v216
	v_and_b32_e32 v216, 0x1ffc0, v216
	v_mov_b32_e32 v217, 0
	v_lshl_add_u64 v[220:221], s[16:17], 0, v[216:217]
	v_lshl_add_u64 v[220:221], v[220:221], 0, v[10:11]
	v_lshl_add_u64 v[216:217], s[10:11], 0, v[216:217]
	v_lshl_add_u64 v[216:217], v[216:217], 0, v[10:11]
	global_load_dwordx4 v[216:219], v[216:217], off
	global_load_dwordx4 v[220:223], v[220:221], off
	v_add_u32_e32 v224, 176, v24
	v_lshlrev_b32_e32 v224, 6, v224
	v_and_b32_e32 v224, 0x1ffc0, v224
	v_mov_b32_e32 v225, 0
	v_lshl_add_u64 v[228:229], s[16:17], 0, v[224:225]
	v_lshl_add_u64 v[228:229], v[228:229], 0, v[10:11]
	v_lshl_add_u64 v[224:225], s[10:11], 0, v[224:225]
	v_lshl_add_u64 v[224:225], v[224:225], 0, v[10:11]
	global_load_dwordx4 v[224:227], v[224:225], off
	global_load_dwordx4 v[228:231], v[228:229], off
	s_branch .LBB0_800

; __device__ __forceinline__ unsigned pk2(float a, float b) { f32x2 v = {a, b}; bf16x2_t r = __builtin_convertvector(v, bf16x2_t); return __builtin_bit_cast(unsigned, r); }
;     __device__ __forceinline__ void operator()(const f32x4 (&acc)[2][2][4][2], const Unit& u, int wr, int wc, int fr, int fq) const {
;     ...
;             for (int m = 0; m < 4; ++m) { const int row = row0 + ai * HALF + m * 16; bf16_t* rowp = O + (size_t)row * ldc + col0;
;                 f32x4 cv = {1.f, 1.f, 1.f, 1.f}, sv = {0.f, 0.f, 0.f, 0.f};
;                 if (rot) { const int pos = row & (T - 1); cv = *(const f32x4*)(rc + pos * 16 + 4 * fq); sv = *(const f32x4*)(rs + pos * 16 + 4 * fq); }
; #pragma unroll
;                 for (int bj = 0; bj < 2; ++bj) { f32x4 v0 = acc[ai][bj][m][0] * sc, v1 = acc[ai][bj][m][1] * sc;
;                     if (rot) { const f32x4 a = v0, b = v1;
;                         v0[0] = a[0] * cv[0] - a[1] * sv[0]; v0[1] = a[0] * sv[0] + a[1] * cv[0]; v0[2] = a[2] * cv[1] - a[3] * sv[1]; v0[3] = a[2] * sv[1] + a[3] * cv[1];
;                         v1[0] = b[0] * cv[2] - b[1] * sv[2]; v1[1] = b[0] * sv[2] + b[1] * cv[2]; v1[2] = b[2] * cv[3] - b[3] * sv[3]; v1[3] = b[2] * sv[3] + b[3] * cv[3]; }
;                     u32x4 w; w.x = pk2(v0[0], v0[1]); w.y = pk2(v0[2], v0[3]); w.z = pk2(v1[0], v1[1]); w.w = pk2(v1[2], v1[3]);
;                     *(u32x4*)(rowp + bj * HALF) = w; } }
.LBB0_802:
	s_lshl_b32 s41, s46, 8
	s_lshl_b32 s39, s39, 5
	s_or_b32 s39, s39, s41
	v_lshl_or_b32 v12, v12, 3, s39
	v_mov_b64_e32 v[14:15], s[22:23]
	v_ashrrev_i32_e32 v13, 31, v12
	v_mad_i64_i32 v[14:15], s[48:49], v24, s63, v[14:15]
	v_lshl_add_u64 v[14:15], v[12:13], 1, v[14:15]
	v_cvt_pk_bf16_f32 v16, v16, v17
	v_cvt_pk_bf16_f32 v17, v22, v23
	v_cvt_pk_bf16_f32 v18, v18, v19
	v_cvt_pk_bf16_f32 v19, v20, v21
	global_store_dwordx4 v[14:15], v[16:19], off
	v_pk_mul_f32 v[22:23], v[152:153], s[36:37] op_sel_hi:[1,0]
	v_pk_mul_f32 v[20:21], v[148:149], s[36:37] op_sel_hi:[1,0]
	v_pk_mul_f32 v[16:17], v[150:151], s[36:37] op_sel_hi:[1,0]
	s_and_b64 vcc, exec, s[8:9]
	v_pk_mul_f32 v[18:19], v[146:147], s[36:37] op_sel_hi:[1,0]
	s_cbranch_vccnz .LBB0_804
	v_pk_mul_f32 v[26:27], v[16:17], v[6:7] op_sel:[1,0] op_sel_hi:[0,0]
	v_mov_b32_e32 v6, v3
	v_mul_f32_e32 v0, v23, v7
	v_pk_mul_f32 v[28:29], v[16:17], v[2:3]
	v_pk_fma_f32 v[16:17], v[16:17], v[2:3], v[26:27] op_sel_hi:[1,0,1]
	v_pk_fma_f32 v[30:31], v[22:23], v[6:7], v[0:1] op_sel_hi:[1,1,0] neg_lo:[0,0,1] neg_hi:[0,0,1]
	v_mov_b32_e32 v2, v7
	v_mul_f32_e32 v0, v23, v3
	v_pk_fma_f32 v[2:3], v[22:23], v[2:3], v[0:1] op_sel_hi:[1,1,0]
	v_pk_mul_f32 v[6:7], v[18:19], v[8:9] op_sel:[1,0] op_sel_hi:[0,0]
	v_mov_b32_e32 v8, v5
	v_mul_f32_e32 v0, v21, v9
	v_pk_mul_f32 v[22:23], v[18:19], v[4:5]
	v_pk_fma_f32 v[18:19], v[18:19], v[4:5], v[6:7] op_sel_hi:[1,0,1]
	v_pk_fma_f32 v[32:33], v[20:21], v[8:9], v[0:1] op_sel_hi:[1,1,0] neg_lo:[0,0,1] neg_hi:[0,0,1]
	v_mov_b32_e32 v4, v9
	v_mul_f32_e32 v0, v21, v5
	v_pk_fma_f32 v[4:5], v[20:21], v[4:5], v[0:1] op_sel_hi:[1,1,0]
	v_sub_f32_e32 v16, v28, v26
	v_sub_f32_e32 v18, v22, v6
	v_mov_b32_e32 v22, v30
	v_mov_b32_e32 v23, v2
	v_mov_b32_e32 v20, v32
	v_mov_b32_e32 v21, v4
.LBB0_804:
	v_cvt_pk_bf16_f32 v2, v16, v17
	v_cvt_pk_bf16_f32 v3, v22, v23
	v_cvt_pk_bf16_f32 v4, v18, v19
	v_cvt_pk_bf16_f32 v5, v20, v21
	global_store_dwordx4 v[14:15], v[2:5], off offset:256
	s_and_b64 vcc, exec, s[8:9]
	v_or_b32_e32 v14, 16, v24
	s_cbranch_vccnz .LBB0_806
	v_mov_b64_e32 v[2:3], v[176:177]
	v_mov_b64_e32 v[4:5], v[178:179]
	v_mov_b64_e32 v[6:7], v[180:181]
	v_mov_b64_e32 v[8:9], v[182:183]
	s_branch .LBB0_807

; __device__ __forceinline__ unsigned pk2(float a, float b) { f32x2 v = {a, b}; bf16x2_t r = __builtin_convertvector(v, bf16x2_t); return __builtin_bit_cast(unsigned, r); }
;     __device__ __forceinline__ void operator()(const f32x4 (&acc)[2][2][4][2], const Unit& u, int wr, int wc, int fr, int fq) const {
;     ...
;             for (int m = 0; m < 4; ++m) { const int row = row0 + ai * HALF + m * 16; bf16_t* rowp = O + (size_t)row * ldc + col0;
;                 f32x4 cv = {1.f, 1.f, 1.f, 1.f}, sv = {0.f, 0.f, 0.f, 0.f};
;                 if (rot) { const int pos = row & (T - 1); cv = *(const f32x4*)(rc + pos * 16 + 4 * fq); sv = *(const f32x4*)(rs + pos * 16 + 4 * fq); }
; #pragma unroll
;                 for (int bj = 0; bj < 2; ++bj) { f32x4 v0 = acc[ai][bj][m][0] * sc, v1 = acc[ai][bj][m][1] * sc;
;                     if (rot) { const f32x4 a = v0, b = v1;
;                         v0[0] = a[0] * cv[0] - a[1] * sv[0]; v0[1] = a[0] * sv[0] + a[1] * cv[0]; v0[2] = a[2] * cv[1] - a[3] * sv[1]; v0[3] = a[2] * sv[1] + a[3] * cv[1];
;                         v1[0] = b[0] * cv[2] - b[1] * sv[2]; v1[1] = b[0] * sv[2] + b[1] * cv[2]; v1[2] = b[2] * cv[3] - b[3] * sv[3]; v1[3] = b[2] * sv[3] + b[3] * cv[3]; }
;                     u32x4 w; w.x = pk2(v0[0], v0[1]); w.y = pk2(v0[2], v0[3]); w.z = pk2(v1[0], v1[1]); w.w = pk2(v1[2], v1[3]);
;                     *(u32x4*)(rowp + bj * HALF) = w; } }
.LBB0_807:
	v_pk_mul_f32 v[22:23], v[144:145], s[36:37] op_sel_hi:[1,0]
	v_pk_mul_f32 v[16:17], v[142:143], s[36:37] op_sel_hi:[1,0]
	v_pk_mul_f32 v[20:21], v[140:141], s[36:37] op_sel_hi:[1,0]
	s_and_b64 vcc, exec, s[8:9]
	v_pk_mul_f32 v[18:19], v[138:139], s[36:37] op_sel_hi:[1,0]
	s_cbranch_vccnz .LBB0_809
	v_mov_b32_e32 v30, v3
	v_mov_b32_e32 v31, v7
	v_mul_f32_e32 v0, v23, v7
	v_pk_fma_f32 v[30:31], v[22:23], v[30:31], v[0:1] op_sel_hi:[1,1,0] neg_lo:[0,0,1] neg_hi:[0,0,1]
	v_mov_b32_e32 v32, v7
	v_mov_b32_e32 v33, v3
	v_mul_f32_e32 v0, v23, v3
	v_pk_fma_f32 v[32:33], v[22:23], v[32:33], v[0:1] op_sel_hi:[1,1,0]
	v_mov_b32_e32 v140, v5
	v_mov_b32_e32 v141, v9
	v_mul_f32_e32 v0, v21, v9
	v_pk_mul_f32 v[26:27], v[16:17], v[6:7] op_sel:[1,0] op_sel_hi:[0,0]
	v_pk_mul_f32 v[22:23], v[18:19], v[8:9] op_sel:[1,0] op_sel_hi:[0,0]
	v_pk_fma_f32 v[140:141], v[20:21], v[140:141], v[0:1] op_sel_hi:[1,1,0] neg_lo:[0,0,1] neg_hi:[0,0,1]
	v_mov_b32_e32 v142, v9
	v_mov_b32_e32 v143, v5
	v_mul_f32_e32 v0, v21, v5
	v_pk_mul_f32 v[28:29], v[16:17], v[2:3]
	v_pk_fma_f32 v[16:17], v[16:17], v[2:3], v[26:27] op_sel_hi:[1,0,1]
	v_pk_mul_f32 v[138:139], v[18:19], v[4:5]
	v_pk_fma_f32 v[18:19], v[18:19], v[4:5], v[22:23] op_sel_hi:[1,0,1]
	v_pk_fma_f32 v[142:143], v[20:21], v[142:143], v[0:1] op_sel_hi:[1,1,0]
	v_sub_f32_e32 v16, v28, v26
	v_sub_f32_e32 v18, v138, v22
	v_mov_b32_e32 v22, v30
	v_mov_b32_e32 v23, v32
	v_mov_b32_e32 v20, v140
	v_mov_b32_e32 v21, v142
.LBB0_809:
	v_mov_b64_e32 v[26:27], s[22:23]
	v_mad_i64_i32 v[14:15], s[48:49], v14, s63, v[26:27]
	v_lshl_add_u64 v[14:15], v[12:13], 1, v[14:15]
	v_cvt_pk_bf16_f32 v16, v16, v17
	v_cvt_pk_bf16_f32 v17, v22, v23
	v_cvt_pk_bf16_f32 v18, v18, v19
	v_cvt_pk_bf16_f32 v19, v20, v21
	global_store_dwordx4 v[14:15], v[16:19], off
	v_pk_mul_f32 v[22:23], v[136:137], s[36:37] op_sel_hi:[1,0]
	v_pk_mul_f32 v[20:21], v[132:133], s[36:37] op_sel_hi:[1,0]
	v_pk_mul_f32 v[16:17], v[134:135], s[36:37] op_sel_hi:[1,0]
	s_and_b64 vcc, exec, s[8:9]
	v_pk_mul_f32 v[18:19], v[130:131], s[36:37] op_sel_hi:[1,0]
	s_cbranch_vccnz .LBB0_811
	v_pk_mul_f32 v[26:27], v[16:17], v[6:7] op_sel:[1,0] op_sel_hi:[0,0]
	v_mov_b32_e32 v6, v3
	v_mul_f32_e32 v0, v23, v7
	v_pk_mul_f32 v[28:29], v[16:17], v[2:3]
	v_pk_fma_f32 v[16:17], v[16:17], v[2:3], v[26:27] op_sel_hi:[1,0,1]
	v_pk_fma_f32 v[30:31], v[22:23], v[6:7], v[0:1] op_sel_hi:[1,1,0] neg_lo:[0,0,1] neg_hi:[0,0,1]
	v_mov_b32_e32 v2, v7
	v_mul_f32_e32 v0, v23, v3
	v_pk_fma_f32 v[2:3], v[22:23], v[2:3], v[0:1] op_sel_hi:[1,1,0]
	v_pk_mul_f32 v[6:7], v[18:19], v[8:9] op_sel:[1,0] op_sel_hi:[0,0]
	v_mov_b32_e32 v8, v5
	v_mul_f32_e32 v0, v21, v9
	v_pk_mul_f32 v[22:23], v[18:19], v[4:5]
	v_pk_fma_f32 v[18:19], v[18:19], v[4:5], v[6:7] op_sel_hi:[1,0,1]
	v_pk_fma_f32 v[32:33], v[20:21], v[8:9], v[0:1] op_sel_hi:[1,1,0] neg_lo:[0,0,1] neg_hi:[0,0,1]
	v_mov_b32_e32 v4, v9
	v_mul_f32_e32 v0, v21, v5
	v_pk_fma_f32 v[4:5], v[20:21], v[4:5], v[0:1] op_sel_hi:[1,1,0]
	v_sub_f32_e32 v16, v28, v26
	v_sub_f32_e32 v18, v22, v6
	v_mov_b32_e32 v22, v30
	v_mov_b32_e32 v23, v2
	v_mov_b32_e32 v20, v32
	v_mov_b32_e32 v21, v4
.LBB0_811:
	v_cvt_pk_bf16_f32 v2, v16, v17
	v_cvt_pk_bf16_f32 v3, v22, v23
	v_cvt_pk_bf16_f32 v4, v18, v19
	v_cvt_pk_bf16_f32 v5, v20, v21
	global_store_dwordx4 v[14:15], v[2:5], off offset:256
	s_and_b64 vcc, exec, s[8:9]
	v_or_b32_e32 v14, 32, v24
	s_cbranch_vccnz .LBB0_813
	v_mov_b64_e32 v[2:3], v[184:185]
	v_mov_b64_e32 v[4:5], v[186:187]
	v_mov_b64_e32 v[6:7], v[188:189]
	v_mov_b64_e32 v[8:9], v[190:191]
	s_branch .LBB0_814

; __device__ __forceinline__ unsigned pk2(float a, float b) { f32x2 v = {a, b}; bf16x2_t r = __builtin_convertvector(v, bf16x2_t); return __builtin_bit_cast(unsigned, r); }
;     __device__ __forceinline__ void operator()(const f32x4 (&acc)[2][2][4][2], const Unit& u, int wr, int wc, int fr, int fq) const {
;     ...
;             for (int m = 0; m < 4; ++m) { const int row = row0 + ai * HALF + m * 16; bf16_t* rowp = O + (size_t)row * ldc + col0;
;                 f32x4 cv = {1.f, 1.f, 1.f, 1.f}, sv = {0.f, 0.f, 0.f, 0.f};
;                 if (rot) { const int pos = row & (T - 1); cv = *(const f32x4*)(rc + pos * 16 + 4 * fq); sv = *(const f32x4*)(rs + pos * 16 + 4 * fq); }
; #pragma unroll
;                 for (int bj = 0; bj < 2; ++bj) { f32x4 v0 = acc[ai][bj][m][0] * sc, v1 = acc[ai][bj][m][1] * sc;
;                     if (rot) { const f32x4 a = v0, b = v1;
;                         v0[0] = a[0] * cv[0] - a[1] * sv[0]; v0[1] = a[0] * sv[0] + a[1] * cv[0]; v0[2] = a[2] * cv[1] - a[3] * sv[1]; v0[3] = a[2] * sv[1] + a[3] * cv[1];
;                         v1[0] = b[0] * cv[2] - b[1] * sv[2]; v1[1] = b[0] * sv[2] + b[1] * cv[2]; v1[2] = b[2] * cv[3] - b[3] * sv[3]; v1[3] = b[2] * sv[3] + b[3] * cv[3]; }
;                     u32x4 w; w.x = pk2(v0[0], v0[1]); w.y = pk2(v0[2], v0[3]); w.z = pk2(v1[0], v1[1]); w.w = pk2(v1[2], v1[3]);
;                     *(u32x4*)(rowp + bj * HALF) = w; } }
.LBB0_814:
	v_pk_mul_f32 v[22:23], v[128:129], s[36:37] op_sel_hi:[1,0]
	v_pk_mul_f32 v[16:17], v[126:127], s[36:37] op_sel_hi:[1,0]
	v_pk_mul_f32 v[20:21], v[124:125], s[36:37] op_sel_hi:[1,0]
	s_and_b64 vcc, exec, s[8:9]
	v_pk_mul_f32 v[18:19], v[122:123], s[36:37] op_sel_hi:[1,0]
	s_cbranch_vccnz .LBB0_816
	v_mov_b32_e32 v30, v3
	v_mov_b32_e32 v31, v7
	v_mul_f32_e32 v0, v23, v7
	v_pk_fma_f32 v[30:31], v[22:23], v[30:31], v[0:1] op_sel_hi:[1,1,0] neg_lo:[0,0,1] neg_hi:[0,0,1]
	v_mov_b32_e32 v32, v7
	v_mov_b32_e32 v33, v3
	v_mul_f32_e32 v0, v23, v3
	v_pk_fma_f32 v[32:33], v[22:23], v[32:33], v[0:1] op_sel_hi:[1,1,0]
	v_mov_b32_e32 v124, v5
	v_mov_b32_e32 v125, v9
	v_mul_f32_e32 v0, v21, v9
	v_pk_mul_f32 v[26:27], v[16:17], v[6:7] op_sel:[1,0] op_sel_hi:[0,0]
	v_pk_mul_f32 v[22:23], v[18:19], v[8:9] op_sel:[1,0] op_sel_hi:[0,0]
	v_pk_fma_f32 v[124:125], v[20:21], v[124:125], v[0:1] op_sel_hi:[1,1,0] neg_lo:[0,0,1] neg_hi:[0,0,1]
	v_mov_b32_e32 v126, v9
	v_mov_b32_e32 v127, v5
	v_mul_f32_e32 v0, v21, v5
	v_pk_mul_f32 v[28:29], v[16:17], v[2:3]
	v_pk_fma_f32 v[16:17], v[16:17], v[2:3], v[26:27] op_sel_hi:[1,0,1]
	v_pk_mul_f32 v[122:123], v[18:19], v[4:5]
	v_pk_fma_f32 v[18:19], v[18:19], v[4:5], v[22:23] op_sel_hi:[1,0,1]
	v_pk_fma_f32 v[126:127], v[20:21], v[126:127], v[0:1] op_sel_hi:[1,1,0]
	v_sub_f32_e32 v16, v28, v26
	v_sub_f32_e32 v18, v122, v22
	v_mov_b32_e32 v22, v30
	v_mov_b32_e32 v23, v32
	v_mov_b32_e32 v20, v124
	v_mov_b32_e32 v21, v126
.LBB0_816:
	v_mov_b64_e32 v[26:27], s[22:23]
	v_mad_i64_i32 v[14:15], s[48:49], v14, s63, v[26:27]
	v_lshl_add_u64 v[14:15], v[12:13], 1, v[14:15]
	v_cvt_pk_bf16_f32 v16, v16, v17
	v_cvt_pk_bf16_f32 v17, v22, v23
	v_cvt_pk_bf16_f32 v18, v18, v19
	v_cvt_pk_bf16_f32 v19, v20, v21
	global_store_dwordx4 v[14:15], v[16:19], off
	v_pk_mul_f32 v[22:23], v[120:121], s[36:37] op_sel_hi:[1,0]
	v_pk_mul_f32 v[20:21], v[116:117], s[36:37] op_sel_hi:[1,0]
	v_pk_mul_f32 v[16:17], v[118:119], s[36:37] op_sel_hi:[1,0]
	s_and_b64 vcc, exec, s[8:9]
	v_pk_mul_f32 v[18:19], v[114:115], s[36:37] op_sel_hi:[1,0]
	s_cbranch_vccnz .LBB0_818
	v_pk_mul_f32 v[26:27], v[16:17], v[6:7] op_sel:[1,0] op_sel_hi:[0,0]
	v_mov_b32_e32 v6, v3
	v_mul_f32_e32 v0, v23, v7
	v_pk_mul_f32 v[28:29], v[16:17], v[2:3]
	v_pk_fma_f32 v[16:17], v[16:17], v[2:3], v[26:27] op_sel_hi:[1,0,1]
	v_pk_fma_f32 v[30:31], v[22:23], v[6:7], v[0:1] op_sel_hi:[1,1,0] neg_lo:[0,0,1] neg_hi:[0,0,1]
	v_mov_b32_e32 v2, v7
	v_mul_f32_e32 v0, v23, v3
	v_pk_fma_f32 v[2:3], v[22:23], v[2:3], v[0:1] op_sel_hi:[1,1,0]
	v_pk_mul_f32 v[6:7], v[18:19], v[8:9] op_sel:[1,0] op_sel_hi:[0,0]
	v_mov_b32_e32 v8, v5
	v_mul_f32_e32 v0, v21, v9
	v_pk_mul_f32 v[22:23], v[18:19], v[4:5]
	v_pk_fma_f32 v[18:19], v[18:19], v[4:5], v[6:7] op_sel_hi:[1,0,1]
	v_pk_fma_f32 v[32:33], v[20:21], v[8:9], v[0:1] op_sel_hi:[1,1,0] neg_lo:[0,0,1] neg_hi:[0,0,1]
	v_mov_b32_e32 v4, v9
	v_mul_f32_e32 v0, v21, v5
	v_pk_fma_f32 v[4:5], v[20:21], v[4:5], v[0:1] op_sel_hi:[1,1,0]
	v_sub_f32_e32 v16, v28, v26
	v_sub_f32_e32 v18, v22, v6
	v_mov_b32_e32 v22, v30
	v_mov_b32_e32 v23, v2
	v_mov_b32_e32 v20, v32
	v_mov_b32_e32 v21, v4
.LBB0_818:
	v_cvt_pk_bf16_f32 v2, v16, v17
	v_cvt_pk_bf16_f32 v3, v22, v23
	v_cvt_pk_bf16_f32 v4, v18, v19
	v_cvt_pk_bf16_f32 v5, v20, v21
	global_store_dwordx4 v[14:15], v[2:5], off offset:256
	s_and_b64 vcc, exec, s[8:9]
	v_or_b32_e32 v14, 48, v24
	s_cbranch_vccnz .LBB0_820
	v_mov_b64_e32 v[2:3], v[192:193]
	v_mov_b64_e32 v[4:5], v[194:195]
	v_mov_b64_e32 v[6:7], v[196:197]
	v_mov_b64_e32 v[8:9], v[198:199]
	s_branch .LBB0_821

; __device__ __forceinline__ unsigned pk2(float a, float b) { f32x2 v = {a, b}; bf16x2_t r = __builtin_convertvector(v, bf16x2_t); return __builtin_bit_cast(unsigned, r); }
;     __device__ __forceinline__ void operator()(const f32x4 (&acc)[2][2][4][2], const Unit& u, int wr, int wc, int fr, int fq) const {
;     ...
;             for (int m = 0; m < 4; ++m) { const int row = row0 + ai * HALF + m * 16; bf16_t* rowp = O + (size_t)row * ldc + col0;
;                 f32x4 cv = {1.f, 1.f, 1.f, 1.f}, sv = {0.f, 0.f, 0.f, 0.f};
;                 if (rot) { const int pos = row & (T - 1); cv = *(const f32x4*)(rc + pos * 16 + 4 * fq); sv = *(const f32x4*)(rs + pos * 16 + 4 * fq); }
; #pragma unroll
;                 for (int bj = 0; bj < 2; ++bj) { f32x4 v0 = acc[ai][bj][m][0] * sc, v1 = acc[ai][bj][m][1] * sc;
;                     if (rot) { const f32x4 a = v0, b = v1;
;                         v0[0] = a[0] * cv[0] - a[1] * sv[0]; v0[1] = a[0] * sv[0] + a[1] * cv[0]; v0[2] = a[2] * cv[1] - a[3] * sv[1]; v0[3] = a[2] * sv[1] + a[3] * cv[1];
;                         v1[0] = b[0] * cv[2] - b[1] * sv[2]; v1[1] = b[0] * sv[2] + b[1] * cv[2]; v1[2] = b[2] * cv[3] - b[3] * sv[3]; v1[3] = b[2] * sv[3] + b[3] * cv[3]; }
;                     u32x4 w; w.x = pk2(v0[0], v0[1]); w.y = pk2(v0[2], v0[3]); w.z = pk2(v1[0], v1[1]); w.w = pk2(v1[2], v1[3]);
;                     *(u32x4*)(rowp + bj * HALF) = w; } }
.LBB0_821:
	v_pk_mul_f32 v[22:23], v[112:113], s[36:37] op_sel_hi:[1,0]
	v_pk_mul_f32 v[16:17], v[110:111], s[36:37] op_sel_hi:[1,0]
	v_pk_mul_f32 v[20:21], v[108:109], s[36:37] op_sel_hi:[1,0]
	s_and_b64 vcc, exec, s[8:9]
	v_pk_mul_f32 v[18:19], v[106:107], s[36:37] op_sel_hi:[1,0]
	s_cbranch_vccnz .LBB0_823
	v_mov_b32_e32 v30, v3
	v_mov_b32_e32 v31, v7
	v_mul_f32_e32 v0, v23, v7
	v_pk_fma_f32 v[30:31], v[22:23], v[30:31], v[0:1] op_sel_hi:[1,1,0] neg_lo:[0,0,1] neg_hi:[0,0,1]
	v_mov_b32_e32 v32, v7
	v_mov_b32_e32 v33, v3
	v_mul_f32_e32 v0, v23, v3
	v_pk_fma_f32 v[32:33], v[22:23], v[32:33], v[0:1] op_sel_hi:[1,1,0]
	v_mov_b32_e32 v108, v5
	v_mov_b32_e32 v109, v9
	v_mul_f32_e32 v0, v21, v9
	v_pk_mul_f32 v[26:27], v[16:17], v[6:7] op_sel:[1,0] op_sel_hi:[0,0]
	v_pk_mul_f32 v[22:23], v[18:19], v[8:9] op_sel:[1,0] op_sel_hi:[0,0]
	v_pk_fma_f32 v[108:109], v[20:21], v[108:109], v[0:1] op_sel_hi:[1,1,0] neg_lo:[0,0,1] neg_hi:[0,0,1]
	v_mov_b32_e32 v110, v9
	v_mov_b32_e32 v111, v5
	v_mul_f32_e32 v0, v21, v5
	v_pk_mul_f32 v[28:29], v[16:17], v[2:3]
	v_pk_fma_f32 v[16:17], v[16:17], v[2:3], v[26:27] op_sel_hi:[1,0,1]
	v_pk_mul_f32 v[106:107], v[18:19], v[4:5]
	v_pk_fma_f32 v[18:19], v[18:19], v[4:5], v[22:23] op_sel_hi:[1,0,1]
	v_pk_fma_f32 v[110:111], v[20:21], v[110:111], v[0:1] op_sel_hi:[1,1,0]
	v_sub_f32_e32 v16, v28, v26
	v_sub_f32_e32 v18, v106, v22
	v_mov_b32_e32 v22, v30
	v_mov_b32_e32 v23, v32
	v_mov_b32_e32 v20, v108
	v_mov_b32_e32 v21, v110
.LBB0_823:
	v_mov_b64_e32 v[26:27], s[22:23]
	v_mad_i64_i32 v[14:15], s[48:49], v14, s63, v[26:27]
	v_lshl_add_u64 v[14:15], v[12:13], 1, v[14:15]
	v_cvt_pk_bf16_f32 v16, v16, v17
	v_cvt_pk_bf16_f32 v17, v22, v23
	v_cvt_pk_bf16_f32 v18, v18, v19
	v_cvt_pk_bf16_f32 v19, v20, v21
	global_store_dwordx4 v[14:15], v[16:19], off
	v_pk_mul_f32 v[22:23], v[104:105], s[36:37] op_sel_hi:[1,0]
	v_pk_mul_f32 v[20:21], v[100:101], s[36:37] op_sel_hi:[1,0]
	v_pk_mul_f32 v[16:17], v[102:103], s[36:37] op_sel_hi:[1,0]
	s_and_b64 vcc, exec, s[8:9]
	v_pk_mul_f32 v[18:19], v[98:99], s[36:37] op_sel_hi:[1,0]
	s_cbranch_vccnz .LBB0_825
	v_pk_mul_f32 v[26:27], v[16:17], v[6:7] op_sel:[1,0] op_sel_hi:[0,0]
	v_mov_b32_e32 v6, v3
	v_mul_f32_e32 v0, v23, v7
	v_pk_mul_f32 v[28:29], v[16:17], v[2:3]
	v_pk_fma_f32 v[16:17], v[16:17], v[2:3], v[26:27] op_sel_hi:[1,0,1]
	v_pk_fma_f32 v[30:31], v[22:23], v[6:7], v[0:1] op_sel_hi:[1,1,0] neg_lo:[0,0,1] neg_hi:[0,0,1]
	v_mov_b32_e32 v2, v7
	v_mul_f32_e32 v0, v23, v3
	v_pk_fma_f32 v[2:3], v[22:23], v[2:3], v[0:1] op_sel_hi:[1,1,0]
	v_pk_mul_f32 v[6:7], v[18:19], v[8:9] op_sel:[1,0] op_sel_hi:[0,0]
	v_mov_b32_e32 v8, v5
	v_mul_f32_e32 v0, v21, v9
	v_pk_mul_f32 v[22:23], v[18:19], v[4:5]
	v_pk_fma_f32 v[18:19], v[18:19], v[4:5], v[6:7] op_sel_hi:[1,0,1]
	v_pk_fma_f32 v[32:33], v[20:21], v[8:9], v[0:1] op_sel_hi:[1,1,0] neg_lo:[0,0,1] neg_hi:[0,0,1]
	v_mov_b32_e32 v4, v9
	v_mul_f32_e32 v0, v21, v5
	v_pk_fma_f32 v[4:5], v[20:21], v[4:5], v[0:1] op_sel_hi:[1,1,0]
	v_sub_f32_e32 v16, v28, v26
	v_sub_f32_e32 v18, v22, v6
	v_mov_b32_e32 v22, v30
	v_mov_b32_e32 v23, v2
	v_mov_b32_e32 v20, v32
	v_mov_b32_e32 v21, v4
.LBB0_825:
	v_cvt_pk_bf16_f32 v2, v16, v17
	v_cvt_pk_bf16_f32 v3, v22, v23
	v_cvt_pk_bf16_f32 v4, v18, v19
	v_cvt_pk_bf16_f32 v5, v20, v21
	global_store_dwordx4 v[14:15], v[2:5], off offset:256
	s_and_b64 vcc, exec, s[8:9]
	v_add_u32_e32 v14, 0x80, v24
	s_cbranch_vccnz .LBB0_827
	v_mov_b64_e32 v[2:3], v[200:201]
	v_mov_b64_e32 v[4:5], v[202:203]
	v_mov_b64_e32 v[6:7], v[204:205]
	v_mov_b64_e32 v[8:9], v[206:207]
	s_branch .LBB0_828

; __device__ __forceinline__ unsigned pk2(float a, float b) { f32x2 v = {a, b}; bf16x2_t r = __builtin_convertvector(v, bf16x2_t); return __builtin_bit_cast(unsigned, r); }
;     __device__ __forceinline__ void operator()(const f32x4 (&acc)[2][2][4][2], const Unit& u, int wr, int wc, int fr, int fq) const {
;     ...
;             for (int m = 0; m < 4; ++m) { const int row = row0 + ai * HALF + m * 16; bf16_t* rowp = O + (size_t)row * ldc + col0;
;                 f32x4 cv = {1.f, 1.f, 1.f, 1.f}, sv = {0.f, 0.f, 0.f, 0.f};
;                 if (rot) { const int pos = row & (T - 1); cv = *(const f32x4*)(rc + pos * 16 + 4 * fq); sv = *(const f32x4*)(rs + pos * 16 + 4 * fq); }
; #pragma unroll
;                 for (int bj = 0; bj < 2; ++bj) { f32x4 v0 = acc[ai][bj][m][0] * sc, v1 = acc[ai][bj][m][1] * sc;
;                     if (rot) { const f32x4 a = v0, b = v1;
;                         v0[0] = a[0] * cv[0] - a[1] * sv[0]; v0[1] = a[0] * sv[0] + a[1] * cv[0]; v0[2] = a[2] * cv[1] - a[3] * sv[1]; v0[3] = a[2] * sv[1] + a[3] * cv[1];
;                         v1[0] = b[0] * cv[2] - b[1] * sv[2]; v1[1] = b[0] * sv[2] + b[1] * cv[2]; v1[2] = b[2] * cv[3] - b[3] * sv[3]; v1[3] = b[2] * sv[3] + b[3] * cv[3]; }
;                     u32x4 w; w.x = pk2(v0[0], v0[1]); w.y = pk2(v0[2], v0[3]); w.z = pk2(v1[0], v1[1]); w.w = pk2(v1[2], v1[3]);
;                     *(u32x4*)(rowp + bj * HALF) = w; } }
.LBB0_828:
	v_pk_mul_f32 v[22:23], v[96:97], s[36:37] op_sel_hi:[1,0]
	v_pk_mul_f32 v[16:17], v[94:95], s[36:37] op_sel_hi:[1,0]
	v_pk_mul_f32 v[20:21], v[92:93], s[36:37] op_sel_hi:[1,0]
	s_and_b64 vcc, exec, s[8:9]
	v_pk_mul_f32 v[18:19], v[90:91], s[36:37] op_sel_hi:[1,0]
	s_cbranch_vccnz .LBB0_830
	v_mov_b32_e32 v30, v3
	v_mov_b32_e32 v31, v7
	v_mul_f32_e32 v0, v23, v7
	v_pk_fma_f32 v[30:31], v[22:23], v[30:31], v[0:1] op_sel_hi:[1,1,0] neg_lo:[0,0,1] neg_hi:[0,0,1]
	v_mov_b32_e32 v32, v7
	v_mov_b32_e32 v33, v3
	v_mul_f32_e32 v0, v23, v3
	v_pk_fma_f32 v[32:33], v[22:23], v[32:33], v[0:1] op_sel_hi:[1,1,0]
	v_mov_b32_e32 v92, v5
	v_mov_b32_e32 v93, v9
	v_mul_f32_e32 v0, v21, v9
	v_pk_mul_f32 v[26:27], v[16:17], v[6:7] op_sel:[1,0] op_sel_hi:[0,0]
	v_pk_mul_f32 v[22:23], v[18:19], v[8:9] op_sel:[1,0] op_sel_hi:[0,0]
	v_pk_fma_f32 v[92:93], v[20:21], v[92:93], v[0:1] op_sel_hi:[1,1,0] neg_lo:[0,0,1] neg_hi:[0,0,1]
	v_mov_b32_e32 v94, v9
	v_mov_b32_e32 v95, v5
	v_mul_f32_e32 v0, v21, v5
	v_pk_mul_f32 v[28:29], v[16:17], v[2:3]
	v_pk_fma_f32 v[16:17], v[16:17], v[2:3], v[26:27] op_sel_hi:[1,0,1]
	v_pk_mul_f32 v[90:91], v[18:19], v[4:5]
	v_pk_fma_f32 v[18:19], v[18:19], v[4:5], v[22:23] op_sel_hi:[1,0,1]
	v_pk_fma_f32 v[94:95], v[20:21], v[94:95], v[0:1] op_sel_hi:[1,1,0]
	v_sub_f32_e32 v16, v28, v26
	v_sub_f32_e32 v18, v90, v22
	v_mov_b32_e32 v22, v30
	v_mov_b32_e32 v23, v32
	v_mov_b32_e32 v20, v92
	v_mov_b32_e32 v21, v94
.LBB0_830:
	v_mov_b64_e32 v[26:27], s[22:23]
	v_mad_i64_i32 v[14:15], s[48:49], v14, s63, v[26:27]
	v_lshl_add_u64 v[14:15], v[12:13], 1, v[14:15]
	v_cvt_pk_bf16_f32 v16, v16, v17
	v_cvt_pk_bf16_f32 v17, v22, v23
	v_cvt_pk_bf16_f32 v18, v18, v19
	v_cvt_pk_bf16_f32 v19, v20, v21
	global_store_dwordx4 v[14:15], v[16:19], off
	v_pk_mul_f32 v[22:23], v[88:89], s[36:37] op_sel_hi:[1,0]
	v_pk_mul_f32 v[20:21], v[84:85], s[36:37] op_sel_hi:[1,0]
	v_pk_mul_f32 v[16:17], v[86:87], s[36:37] op_sel_hi:[1,0]
	s_and_b64 vcc, exec, s[8:9]
	v_pk_mul_f32 v[18:19], v[82:83], s[36:37] op_sel_hi:[1,0]
	s_cbranch_vccnz .LBB0_832
	v_pk_mul_f32 v[26:27], v[16:17], v[6:7] op_sel:[1,0] op_sel_hi:[0,0]
	v_mov_b32_e32 v6, v3
	v_mul_f32_e32 v0, v23, v7
	v_pk_mul_f32 v[28:29], v[16:17], v[2:3]
	v_pk_fma_f32 v[16:17], v[16:17], v[2:3], v[26:27] op_sel_hi:[1,0,1]
	v_pk_fma_f32 v[30:31], v[22:23], v[6:7], v[0:1] op_sel_hi:[1,1,0] neg_lo:[0,0,1] neg_hi:[0,0,1]
	v_mov_b32_e32 v2, v7
	v_mul_f32_e32 v0, v23, v3
	v_pk_fma_f32 v[2:3], v[22:23], v[2:3], v[0:1] op_sel_hi:[1,1,0]
	v_pk_mul_f32 v[6:7], v[18:19], v[8:9] op_sel:[1,0] op_sel_hi:[0,0]
	v_mov_b32_e32 v8, v5
	v_mul_f32_e32 v0, v21, v9
	v_pk_mul_f32 v[22:23], v[18:19], v[4:5]
	v_pk_fma_f32 v[18:19], v[18:19], v[4:5], v[6:7] op_sel_hi:[1,0,1]
	v_pk_fma_f32 v[32:33], v[20:21], v[8:9], v[0:1] op_sel_hi:[1,1,0] neg_lo:[0,0,1] neg_hi:[0,0,1]
	v_mov_b32_e32 v4, v9
	v_mul_f32_e32 v0, v21, v5
	v_pk_fma_f32 v[4:5], v[20:21], v[4:5], v[0:1] op_sel_hi:[1,1,0]
	v_sub_f32_e32 v16, v28, v26
	v_sub_f32_e32 v18, v22, v6
	v_mov_b32_e32 v22, v30
	v_mov_b32_e32 v23, v2
	v_mov_b32_e32 v20, v32
	v_mov_b32_e32 v21, v4
.LBB0_832:
	v_cvt_pk_bf16_f32 v2, v16, v17
	v_cvt_pk_bf16_f32 v3, v22, v23
	v_cvt_pk_bf16_f32 v4, v18, v19
	v_cvt_pk_bf16_f32 v5, v20, v21
	global_store_dwordx4 v[14:15], v[2:5], off offset:256
	s_and_b64 vcc, exec, s[8:9]
	v_add_u32_e32 v14, 0x90, v24
	s_cbranch_vccnz .LBB0_834
	v_mov_b64_e32 v[2:3], v[208:209]
	v_mov_b64_e32 v[4:5], v[210:211]
	v_mov_b64_e32 v[6:7], v[212:213]
	v_mov_b64_e32 v[8:9], v[214:215]
	s_branch .LBB0_835

; __device__ __forceinline__ unsigned pk2(float a, float b) { f32x2 v = {a, b}; bf16x2_t r = __builtin_convertvector(v, bf16x2_t); return __builtin_bit_cast(unsigned, r); }
;     __device__ __forceinline__ void operator()(const f32x4 (&acc)[2][2][4][2], const Unit& u, int wr, int wc, int fr, int fq) const {
;     ...
;             for (int m = 0; m < 4; ++m) { const int row = row0 + ai * HALF + m * 16; bf16_t* rowp = O + (size_t)row * ldc + col0;
;                 f32x4 cv = {1.f, 1.f, 1.f, 1.f}, sv = {0.f, 0.f, 0.f, 0.f};
;                 if (rot) { const int pos = row & (T - 1); cv = *(const f32x4*)(rc + pos * 16 + 4 * fq); sv = *(const f32x4*)(rs + pos * 16 + 4 * fq); }
; #pragma unroll
;                 for (int bj = 0; bj < 2; ++bj) { f32x4 v0 = acc[ai][bj][m][0] * sc, v1 = acc[ai][bj][m][1] * sc;
;                     if (rot) { const f32x4 a = v0, b = v1;
;                         v0[0] = a[0] * cv[0] - a[1] * sv[0]; v0[1] = a[0] * sv[0] + a[1] * cv[0]; v0[2] = a[2] * cv[1] - a[3] * sv[1]; v0[3] = a[2] * sv[1] + a[3] * cv[1];
;                         v1[0] = b[0] * cv[2] - b[1] * sv[2]; v1[1] = b[0] * sv[2] + b[1] * cv[2]; v1[2] = b[2] * cv[3] - b[3] * sv[3]; v1[3] = b[2] * sv[3] + b[3] * cv[3]; }
;                     u32x4 w; w.x = pk2(v0[0], v0[1]); w.y = pk2(v0[2], v0[3]); w.z = pk2(v1[0], v1[1]); w.w = pk2(v1[2], v1[3]);
;                     *(u32x4*)(rowp + bj * HALF) = w; } }
.LBB0_835:
	v_pk_mul_f32 v[22:23], v[80:81], s[36:37] op_sel_hi:[1,0]
	v_pk_mul_f32 v[16:17], v[78:79], s[36:37] op_sel_hi:[1,0]
	v_pk_mul_f32 v[20:21], v[76:77], s[36:37] op_sel_hi:[1,0]
	s_and_b64 vcc, exec, s[8:9]
	v_pk_mul_f32 v[18:19], v[74:75], s[36:37] op_sel_hi:[1,0]
	s_cbranch_vccnz .LBB0_837
	v_mov_b32_e32 v30, v3
	v_mov_b32_e32 v31, v7
	v_mul_f32_e32 v0, v23, v7
	v_pk_fma_f32 v[30:31], v[22:23], v[30:31], v[0:1] op_sel_hi:[1,1,0] neg_lo:[0,0,1] neg_hi:[0,0,1]
	v_mov_b32_e32 v32, v7
	v_mov_b32_e32 v33, v3
	v_mul_f32_e32 v0, v23, v3
	v_pk_fma_f32 v[32:33], v[22:23], v[32:33], v[0:1] op_sel_hi:[1,1,0]
	v_mov_b32_e32 v76, v5
	v_mov_b32_e32 v77, v9
	v_mul_f32_e32 v0, v21, v9
	v_pk_mul_f32 v[26:27], v[16:17], v[6:7] op_sel:[1,0] op_sel_hi:[0,0]
	v_pk_mul_f32 v[22:23], v[18:19], v[8:9] op_sel:[1,0] op_sel_hi:[0,0]
	v_pk_fma_f32 v[76:77], v[20:21], v[76:77], v[0:1] op_sel_hi:[1,1,0] neg_lo:[0,0,1] neg_hi:[0,0,1]
	v_mov_b32_e32 v78, v9
	v_mov_b32_e32 v79, v5
	v_mul_f32_e32 v0, v21, v5
	v_pk_mul_f32 v[28:29], v[16:17], v[2:3]
	v_pk_fma_f32 v[16:17], v[16:17], v[2:3], v[26:27] op_sel_hi:[1,0,1]
	v_pk_mul_f32 v[74:75], v[18:19], v[4:5]
	v_pk_fma_f32 v[18:19], v[18:19], v[4:5], v[22:23] op_sel_hi:[1,0,1]
	v_pk_fma_f32 v[78:79], v[20:21], v[78:79], v[0:1] op_sel_hi:[1,1,0]
	v_sub_f32_e32 v16, v28, v26
	v_sub_f32_e32 v18, v74, v22
	v_mov_b32_e32 v22, v30
	v_mov_b32_e32 v23, v32
	v_mov_b32_e32 v20, v76
	v_mov_b32_e32 v21, v78
.LBB0_837:
	v_mov_b64_e32 v[26:27], s[22:23]
	v_mad_i64_i32 v[14:15], s[48:49], v14, s63, v[26:27]
	v_lshl_add_u64 v[14:15], v[12:13], 1, v[14:15]
	v_cvt_pk_bf16_f32 v16, v16, v17
	v_cvt_pk_bf16_f32 v17, v22, v23
	v_cvt_pk_bf16_f32 v18, v18, v19
	v_cvt_pk_bf16_f32 v19, v20, v21
	global_store_dwordx4 v[14:15], v[16:19], off
	v_pk_mul_f32 v[22:23], v[72:73], s[36:37] op_sel_hi:[1,0]
	v_pk_mul_f32 v[20:21], v[68:69], s[36:37] op_sel_hi:[1,0]
	v_pk_mul_f32 v[16:17], v[70:71], s[36:37] op_sel_hi:[1,0]
	s_and_b64 vcc, exec, s[8:9]
	v_pk_mul_f32 v[18:19], v[66:67], s[36:37] op_sel_hi:[1,0]
	s_cbranch_vccnz .LBB0_839
	v_pk_mul_f32 v[26:27], v[16:17], v[6:7] op_sel:[1,0] op_sel_hi:[0,0]
	v_mov_b32_e32 v6, v3
	v_mul_f32_e32 v0, v23, v7
	v_pk_mul_f32 v[28:29], v[16:17], v[2:3]
	v_pk_fma_f32 v[16:17], v[16:17], v[2:3], v[26:27] op_sel_hi:[1,0,1]
	v_pk_fma_f32 v[30:31], v[22:23], v[6:7], v[0:1] op_sel_hi:[1,1,0] neg_lo:[0,0,1] neg_hi:[0,0,1]
	v_mov_b32_e32 v2, v7
	v_mul_f32_e32 v0, v23, v3
	v_pk_fma_f32 v[2:3], v[22:23], v[2:3], v[0:1] op_sel_hi:[1,1,0]
	v_pk_mul_f32 v[6:7], v[18:19], v[8:9] op_sel:[1,0] op_sel_hi:[0,0]
	v_mov_b32_e32 v8, v5
	v_mul_f32_e32 v0, v21, v9
	v_pk_mul_f32 v[22:23], v[18:19], v[4:5]
	v_pk_fma_f32 v[18:19], v[18:19], v[4:5], v[6:7] op_sel_hi:[1,0,1]
	v_pk_fma_f32 v[32:33], v[20:21], v[8:9], v[0:1] op_sel_hi:[1,1,0] neg_lo:[0,0,1] neg_hi:[0,0,1]
	v_mov_b32_e32 v4, v9
	v_mul_f32_e32 v0, v21, v5
	v_pk_fma_f32 v[4:5], v[20:21], v[4:5], v[0:1] op_sel_hi:[1,1,0]
	v_sub_f32_e32 v16, v28, v26
	v_sub_f32_e32 v18, v22, v6
	v_mov_b32_e32 v22, v30
	v_mov_b32_e32 v23, v2
	v_mov_b32_e32 v20, v32
	v_mov_b32_e32 v21, v4
.LBB0_839:
	v_cvt_pk_bf16_f32 v2, v16, v17
	v_cvt_pk_bf16_f32 v3, v22, v23
	v_cvt_pk_bf16_f32 v4, v18, v19
	v_cvt_pk_bf16_f32 v5, v20, v21
	global_store_dwordx4 v[14:15], v[2:5], off offset:256
	s_and_b64 vcc, exec, s[8:9]
	v_add_u32_e32 v14, 0xa0, v24
	s_cbranch_vccnz .LBB0_841
	v_mov_b64_e32 v[2:3], v[216:217]
	v_mov_b64_e32 v[4:5], v[218:219]
	v_mov_b64_e32 v[6:7], v[220:221]
	v_mov_b64_e32 v[8:9], v[222:223]
	s_branch .LBB0_842

; __device__ __forceinline__ unsigned pk2(float a, float b) { f32x2 v = {a, b}; bf16x2_t r = __builtin_convertvector(v, bf16x2_t); return __builtin_bit_cast(unsigned, r); }
;     __device__ __forceinline__ void operator()(const f32x4 (&acc)[2][2][4][2], const Unit& u, int wr, int wc, int fr, int fq) const {
;     ...
;             for (int m = 0; m < 4; ++m) { const int row = row0 + ai * HALF + m * 16; bf16_t* rowp = O + (size_t)row * ldc + col0;
;                 f32x4 cv = {1.f, 1.f, 1.f, 1.f}, sv = {0.f, 0.f, 0.f, 0.f};
;                 if (rot) { const int pos = row & (T - 1); cv = *(const f32x4*)(rc + pos * 16 + 4 * fq); sv = *(const f32x4*)(rs + pos * 16 + 4 * fq); }
; #pragma unroll
;                 for (int bj = 0; bj < 2; ++bj) { f32x4 v0 = acc[ai][bj][m][0] * sc, v1 = acc[ai][bj][m][1] * sc;
;                     if (rot) { const f32x4 a = v0, b = v1;
;                         v0[0] = a[0] * cv[0] - a[1] * sv[0]; v0[1] = a[0] * sv[0] + a[1] * cv[0]; v0[2] = a[2] * cv[1] - a[3] * sv[1]; v0[3] = a[2] * sv[1] + a[3] * cv[1];
;                         v1[0] = b[0] * cv[2] - b[1] * sv[2]; v1[1] = b[0] * sv[2] + b[1] * cv[2]; v1[2] = b[2] * cv[3] - b[3] * sv[3]; v1[3] = b[2] * sv[3] + b[3] * cv[3]; }
;                     u32x4 w; w.x = pk2(v0[0], v0[1]); w.y = pk2(v0[2], v0[3]); w.z = pk2(v1[0], v1[1]); w.w = pk2(v1[2], v1[3]);
;                     *(u32x4*)(rowp + bj * HALF) = w; } }
.LBB0_842:
	v_pk_mul_f32 v[22:23], v[64:65], s[36:37] op_sel_hi:[1,0]
	v_pk_mul_f32 v[16:17], v[62:63], s[36:37] op_sel_hi:[1,0]
	v_pk_mul_f32 v[20:21], v[60:61], s[36:37] op_sel_hi:[1,0]
	s_and_b64 vcc, exec, s[8:9]
	v_pk_mul_f32 v[18:19], v[58:59], s[36:37] op_sel_hi:[1,0]
	s_cbranch_vccnz .LBB0_844
	v_mov_b32_e32 v30, v3
	v_mov_b32_e32 v31, v7
	v_mul_f32_e32 v0, v23, v7
	v_pk_fma_f32 v[30:31], v[22:23], v[30:31], v[0:1] op_sel_hi:[1,1,0] neg_lo:[0,0,1] neg_hi:[0,0,1]
	v_mov_b32_e32 v32, v7
	v_mov_b32_e32 v33, v3
	v_mul_f32_e32 v0, v23, v3
	v_pk_fma_f32 v[32:33], v[22:23], v[32:33], v[0:1] op_sel_hi:[1,1,0]
	v_mov_b32_e32 v60, v5
	v_mov_b32_e32 v61, v9
	v_mul_f32_e32 v0, v21, v9
	v_pk_mul_f32 v[26:27], v[16:17], v[6:7] op_sel:[1,0] op_sel_hi:[0,0]
	v_pk_mul_f32 v[22:23], v[18:19], v[8:9] op_sel:[1,0] op_sel_hi:[0,0]
	v_pk_fma_f32 v[60:61], v[20:21], v[60:61], v[0:1] op_sel_hi:[1,1,0] neg_lo:[0,0,1] neg_hi:[0,0,1]
	v_mov_b32_e32 v62, v9
	v_mov_b32_e32 v63, v5
	v_mul_f32_e32 v0, v21, v5
	v_pk_mul_f32 v[28:29], v[16:17], v[2:3]
	v_pk_fma_f32 v[16:17], v[16:17], v[2:3], v[26:27] op_sel_hi:[1,0,1]
	v_pk_mul_f32 v[58:59], v[18:19], v[4:5]
	v_pk_fma_f32 v[18:19], v[18:19], v[4:5], v[22:23] op_sel_hi:[1,0,1]
	v_pk_fma_f32 v[62:63], v[20:21], v[62:63], v[0:1] op_sel_hi:[1,1,0]
	v_sub_f32_e32 v16, v28, v26
	v_sub_f32_e32 v18, v58, v22
	v_mov_b32_e32 v22, v30
	v_mov_b32_e32 v23, v32
	v_mov_b32_e32 v20, v60
	v_mov_b32_e32 v21, v62
.LBB0_844:
	v_mov_b64_e32 v[26:27], s[22:23]
	v_mad_i64_i32 v[14:15], s[48:49], v14, s63, v[26:27]
	v_lshl_add_u64 v[14:15], v[12:13], 1, v[14:15]
	v_cvt_pk_bf16_f32 v16, v16, v17
	v_cvt_pk_bf16_f32 v17, v22, v23
	v_cvt_pk_bf16_f32 v18, v18, v19
	v_cvt_pk_bf16_f32 v19, v20, v21
	global_store_dwordx4 v[14:15], v[16:19], off
	v_pk_mul_f32 v[22:23], v[56:57], s[36:37] op_sel_hi:[1,0]
	v_pk_mul_f32 v[20:21], v[52:53], s[36:37] op_sel_hi:[1,0]
	v_pk_mul_f32 v[16:17], v[54:55], s[36:37] op_sel_hi:[1,0]
	s_and_b64 vcc, exec, s[8:9]
	v_pk_mul_f32 v[18:19], v[50:51], s[36:37] op_sel_hi:[1,0]
	s_cbranch_vccnz .LBB0_846
	v_pk_mul_f32 v[26:27], v[16:17], v[6:7] op_sel:[1,0] op_sel_hi:[0,0]
	v_mov_b32_e32 v6, v3
	v_mul_f32_e32 v0, v23, v7
	v_pk_mul_f32 v[28:29], v[16:17], v[2:3]
	v_pk_fma_f32 v[16:17], v[16:17], v[2:3], v[26:27] op_sel_hi:[1,0,1]
	v_pk_fma_f32 v[30:31], v[22:23], v[6:7], v[0:1] op_sel_hi:[1,1,0] neg_lo:[0,0,1] neg_hi:[0,0,1]
	v_mov_b32_e32 v2, v7
	v_mul_f32_e32 v0, v23, v3
	v_pk_fma_f32 v[2:3], v[22:23], v[2:3], v[0:1] op_sel_hi:[1,1,0]
	v_pk_mul_f32 v[6:7], v[18:19], v[8:9] op_sel:[1,0] op_sel_hi:[0,0]
	v_mov_b32_e32 v8, v5
	v_mul_f32_e32 v0, v21, v9
	v_pk_mul_f32 v[22:23], v[18:19], v[4:5]
	v_pk_fma_f32 v[18:19], v[18:19], v[4:5], v[6:7] op_sel_hi:[1,0,1]
	v_pk_fma_f32 v[32:33], v[20:21], v[8:9], v[0:1] op_sel_hi:[1,1,0] neg_lo:[0,0,1] neg_hi:[0,0,1]
	v_mov_b32_e32 v4, v9
	v_mul_f32_e32 v0, v21, v5
	v_pk_fma_f32 v[4:5], v[20:21], v[4:5], v[0:1] op_sel_hi:[1,1,0]
	v_sub_f32_e32 v16, v28, v26
	v_sub_f32_e32 v18, v22, v6
	v_mov_b32_e32 v22, v30
	v_mov_b32_e32 v23, v2
	v_mov_b32_e32 v20, v32
	v_mov_b32_e32 v21, v4
.LBB0_846:
	v_cvt_pk_bf16_f32 v2, v16, v17
	v_cvt_pk_bf16_f32 v3, v22, v23
	v_cvt_pk_bf16_f32 v4, v18, v19
	v_cvt_pk_bf16_f32 v5, v20, v21
	s_and_b64 vcc, exec, s[8:9]
	v_add_u32_e32 v22, 0xb0, v24
	global_store_dwordx4 v[14:15], v[2:5], off offset:256
	s_cbranch_vccnz .LBB0_848
	v_mov_b64_e32 v[2:3], v[224:225]
	v_mov_b64_e32 v[4:5], v[226:227]
	v_mov_b64_e32 v[6:7], v[228:229]
	v_mov_b64_e32 v[8:9], v[230:231]
	s_branch .LBB0_849

; __device__ __forceinline__ unsigned pk2(float a, float b) { f32x2 v = {a, b}; bf16x2_t r = __builtin_convertvector(v, bf16x2_t); return __builtin_bit_cast(unsigned, r); }
;     __device__ __forceinline__ void operator()(const f32x4 (&acc)[2][2][4][2], const Unit& u, int wr, int wc, int fr, int fq) const {
;     ...
;             for (int m = 0; m < 4; ++m) { const int row = row0 + ai * HALF + m * 16; bf16_t* rowp = O + (size_t)row * ldc + col0;
;                 f32x4 cv = {1.f, 1.f, 1.f, 1.f}, sv = {0.f, 0.f, 0.f, 0.f};
;                 if (rot) { const int pos = row & (T - 1); cv = *(const f32x4*)(rc + pos * 16 + 4 * fq); sv = *(const f32x4*)(rs + pos * 16 + 4 * fq); }
; #pragma unroll
;                 for (int bj = 0; bj < 2; ++bj) { f32x4 v0 = acc[ai][bj][m][0] * sc, v1 = acc[ai][bj][m][1] * sc;
;                     if (rot) { const f32x4 a = v0, b = v1;
;                         v0[0] = a[0] * cv[0] - a[1] * sv[0]; v0[1] = a[0] * sv[0] + a[1] * cv[0]; v0[2] = a[2] * cv[1] - a[3] * sv[1]; v0[3] = a[2] * sv[1] + a[3] * cv[1];
;                         v1[0] = b[0] * cv[2] - b[1] * sv[2]; v1[1] = b[0] * sv[2] + b[1] * cv[2]; v1[2] = b[2] * cv[3] - b[3] * sv[3]; v1[3] = b[2] * sv[3] + b[3] * cv[3]; }
;                     u32x4 w; w.x = pk2(v0[0], v0[1]); w.y = pk2(v0[2], v0[3]); w.z = pk2(v1[0], v1[1]); w.w = pk2(v1[2], v1[3]);
;                     *(u32x4*)(rowp + bj * HALF) = w; } }
.LBB0_849:
	v_pk_mul_f32 v[20:21], v[48:49], s[36:37] op_sel_hi:[1,0]
	v_pk_mul_f32 v[14:15], v[46:47], s[36:37] op_sel_hi:[1,0]
	v_pk_mul_f32 v[18:19], v[44:45], s[36:37] op_sel_hi:[1,0]
	s_and_b64 vcc, exec, s[8:9]
	v_pk_mul_f32 v[16:17], v[42:43], s[36:37] op_sel_hi:[1,0]
	s_cbranch_vccnz .LBB0_851
	v_mov_b32_e32 v26, v3
	v_mov_b32_e32 v27, v7
	v_mul_f32_e32 v0, v21, v7
	v_pk_fma_f32 v[26:27], v[20:21], v[26:27], v[0:1] op_sel_hi:[1,1,0] neg_lo:[0,0,1] neg_hi:[0,0,1]
	v_mov_b32_e32 v28, v7
	v_mov_b32_e32 v29, v3
	v_mul_f32_e32 v0, v21, v3
	v_pk_fma_f32 v[28:29], v[20:21], v[28:29], v[0:1] op_sel_hi:[1,1,0]
	v_mov_b32_e32 v32, v5
	v_mov_b32_e32 v33, v9
	v_mul_f32_e32 v0, v19, v9
	v_pk_mul_f32 v[10:11], v[14:15], v[6:7] op_sel:[1,0] op_sel_hi:[0,0]
	v_pk_mul_f32 v[20:21], v[16:17], v[8:9] op_sel:[1,0] op_sel_hi:[0,0]
	v_pk_fma_f32 v[32:33], v[18:19], v[32:33], v[0:1] op_sel_hi:[1,1,0] neg_lo:[0,0,1] neg_hi:[0,0,1]
	v_mov_b32_e32 v42, v9
	v_mov_b32_e32 v43, v5
	v_mul_f32_e32 v0, v19, v5
	v_pk_mul_f32 v[24:25], v[14:15], v[2:3]
	v_pk_fma_f32 v[14:15], v[14:15], v[2:3], v[10:11] op_sel_hi:[1,0,1]
	v_pk_mul_f32 v[30:31], v[16:17], v[4:5]
	v_pk_fma_f32 v[16:17], v[16:17], v[4:5], v[20:21] op_sel_hi:[1,0,1]
	v_pk_fma_f32 v[42:43], v[18:19], v[42:43], v[0:1] op_sel_hi:[1,1,0]
	v_sub_f32_e32 v14, v24, v10
	v_sub_f32_e32 v16, v30, v20
	v_mov_b32_e32 v20, v26
	v_mov_b32_e32 v21, v28
	v_mov_b32_e32 v18, v32
	v_mov_b32_e32 v19, v42
.LBB0_851:
	v_mov_b64_e32 v[10:11], s[22:23]
	v_mad_i64_i32 v[10:11], s[48:49], v22, s63, v[10:11]
	v_lshl_add_u64 v[10:11], v[12:13], 1, v[10:11]
	v_cvt_pk_bf16_f32 v12, v14, v15
	v_cvt_pk_bf16_f32 v13, v20, v21
	v_cvt_pk_bf16_f32 v14, v16, v17
	v_cvt_pk_bf16_f32 v15, v18, v19
	global_store_dwordx4 v[10:11], v[12:15], off
	v_pk_mul_f32 v[18:19], v[40:41], s[36:37] op_sel_hi:[1,0]
	v_pk_mul_f32 v[16:17], v[36:37], s[36:37] op_sel_hi:[1,0]
	v_pk_mul_f32 v[12:13], v[38:39], s[36:37] op_sel_hi:[1,0]
	s_and_b64 vcc, exec, s[8:9]
	v_pk_mul_f32 v[14:15], v[34:35], s[36:37] op_sel_hi:[1,0]
	s_cbranch_vccnz .LBB0_853
	v_pk_mul_f32 v[20:21], v[12:13], v[6:7] op_sel:[1,0] op_sel_hi:[0,0]
	v_mov_b32_e32 v6, v3
	v_mul_f32_e32 v0, v19, v7
	v_pk_mul_f32 v[22:23], v[12:13], v[2:3]
	v_pk_fma_f32 v[12:13], v[12:13], v[2:3], v[20:21] op_sel_hi:[1,0,1]
	v_pk_fma_f32 v[24:25], v[18:19], v[6:7], v[0:1] op_sel_hi:[1,1,0] neg_lo:[0,0,1] neg_hi:[0,0,1]
	v_mov_b32_e32 v2, v7
	v_mul_f32_e32 v0, v19, v3
	v_pk_fma_f32 v[2:3], v[18:19], v[2:3], v[0:1] op_sel_hi:[1,1,0]
	v_pk_mul_f32 v[6:7], v[14:15], v[8:9] op_sel:[1,0] op_sel_hi:[0,0]
	v_mov_b32_e32 v8, v5
	v_mul_f32_e32 v0, v17, v9
	v_pk_mul_f32 v[18:19], v[14:15], v[4:5]
	v_pk_fma_f32 v[14:15], v[14:15], v[4:5], v[6:7] op_sel_hi:[1,0,1]
	v_pk_fma_f32 v[26:27], v[16:17], v[8:9], v[0:1] op_sel_hi:[1,1,0] neg_lo:[0,0,1] neg_hi:[0,0,1]
	v_mov_b32_e32 v4, v9
	v_mul_f32_e32 v0, v17, v5
	v_pk_fma_f32 v[4:5], v[16:17], v[4:5], v[0:1] op_sel_hi:[1,1,0]
	v_sub_f32_e32 v12, v22, v20
	v_sub_f32_e32 v14, v18, v6
	v_mov_b32_e32 v18, v24
	v_mov_b32_e32 v19, v2
	v_mov_b32_e32 v16, v26
	v_mov_b32_e32 v17, v4
